# P2 K-loop: streamer load-address VALU + loads moved into MMA1 nop slots, store-address VALU into MMA2 nop slots; load segment keeps only SALU and the four stores
# baseline (speedup 1.0000x reference)
.LBB0_347:
	v_mov_b32_e32 v152, v204
	v_mov_b32_e32 v153, v234
	v_mov_b32_e32 v154, v235
	v_mov_b32_e32 v155, v236
	ds_read_b128 v[158:161], v217
	ds_read_b128 v[162:165], v218
	ds_read_b128 v[166:169], v219
	ds_read_b128 v[170:173], v220
	ds_read_b128 v[148:151], v221
	ds_read_b128 v[144:147], v222
	ds_read_b128 v[140:143], v223
	ds_read_b128 v[136:139], v224
	ds_read_b128 v[174:177], v233
	ds_read_b128 v[178:181], v233 offset:1024
	ds_read_b128 v[182:185], v233 offset:2048
	ds_read_b128 v[186:189], v233 offset:3072
	ds_read_b128 v[190:193], v233 offset:4096
	ds_read_b128 v[194:197], v233 offset:5120
	ds_read_b128 v[234:237], v233 offset:6144
	ds_read_b128 v[238:241], v233 offset:7168
	s_add_i32 s4, s60, s61
	s_mov_b32 s46, s94
	s_add_i32 s94, s94, 1
	s_add_i32 s5, s4, 0x200
	s_add_i32 s16, s33, s61
	s_cmpk_eq_i32 s61, 0x1e00
	s_cselect_b32 s47, s90, s5
	s_cselect_b32 s97, s91, s16
	s_add_i32 s96, s47, 0x80
	s_mov_b32 m0, s82
	s_add_i32 s5, s4, 0x100180
	buffer_load_dwordx4 v214, s[8:11], s5 offen lds
	s_add_i32 s4, s4, 0x180180
	s_mov_b32 m0, s85
	s_add_i32 vcc_lo, s97, 0x80
	buffer_load_dwordx4 v214, s[8:11], s4 offen lds
	s_lshr_b32 s4, s94, 2
	s_mul_i32 s5, s4, s34
	s_add_i32 s16, s5, s2
	s_cmp_lt_i32 s4, s3
	s_cselect_b64 s[4:5], -1, 0
	s_and_b64 s[44:45], s[4:5], exec
	s_cselect_b32 s16, s16, 0
	s_bfe_u32 s17, s94, 0x10001
	s_or_b32 s17, s17, s83
	s_bfe_u32 s67, s16, 0x50007
	s_bfe_u32 s36, s16, 0x50002
	s_and_b32 s95, s16, 3
	s_cmpk_gt_i32 s16, 0xfff
	s_cselect_b64 s[44:45], -1, 0
	v_lshl_or_b32 v156, s17, 3, v216
	s_and_b64 s[16:17], s[44:45], exec
	s_cselect_b32 s16, s25, s21
	s_cselect_b32 s17, s24, s20
	s_lshl_b32 vcc_hi, s67, 23
	s_add_u32 s17, s17, vcc_hi
	s_addc_u32 s16, s16, 0
	s_lshl_b32 vcc_hi, s36, 18
	s_add_u32 s17, s17, vcc_hi
	s_addc_u32 vcc_hi, s16, 0
	s_lshl_b32 s16, s95, 9
	s_add_u32 s16, s17, s16
	s_addc_u32 s17, vcc_hi, 0
	s_waitcnt vmcnt(8)
	s_waitcnt lgkmcnt(8)
	s_barrier
	s_setprio 1
	s_waitcnt lgkmcnt(7)
	v_mfma_f32_16x16x32_bf16 v[124:127], v[158:161], v[174:177], v[124:127]
	s_waitcnt lgkmcnt(6)
	v_mfma_f32_16x16x32_bf16 v[124:127], v[162:165], v[178:181], v[124:127]
	v_mfma_f32_16x16x32_bf16 v[120:123], v[166:169], v[174:177], v[120:123]
	s_nop 0
	v_mfma_f32_16x16x32_bf16 v[120:123], v[170:173], v[178:181], v[120:123]
	s_waitcnt lgkmcnt(5)
	v_mfma_f32_16x16x32_bf16 v[116:119], v[158:161], v[182:185], v[116:119]
	s_waitcnt lgkmcnt(4)
	v_mfma_f32_16x16x32_bf16 v[116:119], v[162:165], v[186:189], v[116:119]
	v_mfma_f32_16x16x32_bf16 v[112:115], v[166:169], v[182:185], v[112:115]
	s_nop 0
	v_mfma_f32_16x16x32_bf16 v[112:115], v[170:173], v[186:189], v[112:115]
	s_waitcnt lgkmcnt(3)
	v_mfma_f32_16x16x32_bf16 v[108:111], v[158:161], v[190:193], v[108:111]
	s_waitcnt lgkmcnt(2)
	v_mfma_f32_16x16x32_bf16 v[108:111], v[162:165], v[194:197], v[108:111]
	v_mfma_f32_16x16x32_bf16 v[104:107], v[166:169], v[190:193], v[104:107]
	s_nop 0
	v_mfma_f32_16x16x32_bf16 v[104:107], v[170:173], v[194:197], v[104:107]
	s_waitcnt lgkmcnt(1)
	v_mfma_f32_16x16x32_bf16 v[100:103], v[158:161], v[234:237], v[100:103]
	s_waitcnt lgkmcnt(0)
	v_mfma_f32_16x16x32_bf16 v[100:103], v[162:165], v[238:241], v[100:103]
	v_mfma_f32_16x16x32_bf16 v[96:99], v[166:169], v[234:237], v[96:99]
	s_nop 0
	v_mfma_f32_16x16x32_bf16 v[96:99], v[170:173], v[238:241], v[96:99]
	s_setprio 0
	s_setprio 1
	v_mfma_f32_16x16x32_bf16 v[92:95], v[148:151], v[174:177], v[92:95]
	v_and_or_b32 v204, s66, 2, v200
	v_mfma_f32_16x16x32_bf16 v[92:95], v[144:147], v[178:181], v[92:95]
	v_mfma_f32_16x16x32_bf16 v[88:91], v[140:143], v[174:177], v[88:91]
	v_lshlrev_b64 v[128:129], 11, v[204:205]
	v_mfma_f32_16x16x32_bf16 v[88:91], v[136:139], v[178:181], v[88:91]
	v_mfma_f32_16x16x32_bf16 v[84:87], v[148:151], v[182:185], v[84:87]
	v_lshl_add_u64 v[128:129], s[16:17], 0, v[128:129]
	v_mfma_f32_16x16x32_bf16 v[84:87], v[144:147], v[186:189], v[84:87]
	v_mfma_f32_16x16x32_bf16 v[80:83], v[140:143], v[182:185], v[80:83]
	v_lshlrev_b32_e32 v204, 4, v156
	v_mfma_f32_16x16x32_bf16 v[80:83], v[136:139], v[186:189], v[80:83]
	v_mfma_f32_16x16x32_bf16 v[76:79], v[148:151], v[190:193], v[76:79]
	v_lshl_add_u64 v[132:133], v[128:129], 0, v[204:205]
	v_mfma_f32_16x16x32_bf16 v[76:79], v[144:147], v[194:197], v[76:79]
	v_mfma_f32_16x16x32_bf16 v[72:75], v[140:143], v[190:193], v[72:75]
	global_load_dwordx4 v[128:131], v[132:133], off nt
	v_mfma_f32_16x16x32_bf16 v[72:75], v[136:139], v[194:197], v[72:75]
	v_mfma_f32_16x16x32_bf16 v[68:71], v[148:151], v[234:237], v[68:71]
	global_load_dwordx4 v[132:135], v[132:133], off offset:2048 nt
	v_mfma_f32_16x16x32_bf16 v[68:71], v[144:147], v[238:241], v[68:71]
	v_mfma_f32_16x16x32_bf16 v[64:67], v[140:143], v[234:237], v[64:67]
	s_nop 0
	v_mfma_f32_16x16x32_bf16 v[64:67], v[136:139], v[238:241], v[64:67]
	s_setprio 0
	s_barrier
	ds_read_b128 v[174:177], v233 offset:16384
	ds_read_b128 v[178:181], v233 offset:17408
	ds_read_b128 v[182:185], v233 offset:18432
	ds_read_b128 v[186:189], v233 offset:19456
	ds_read_b128 v[190:193], v233 offset:20480
	ds_read_b128 v[194:197], v233 offset:21504
	ds_read_b128 v[234:237], v233 offset:22528
	ds_read_b128 v[238:241], v233 offset:23552
	s_mov_b32 m0, s65
	s_add_i32 s16, s97, 0x100000
	buffer_load_dwordx4 v215, s[12:15], s97 offen lds
	s_mov_b32 m0, s68
	s_nop 0
	buffer_load_dwordx4 v215, s[12:15], s16 offen lds
	s_add_i32 s16, s97, 0x10000
	s_mov_b32 m0, s69
	s_nop 0
	buffer_load_dwordx4 v215, s[12:15], s16 offen lds
	s_add_i32 s16, s97, 0x110000
	s_mov_b32 m0, s70
	s_nop 0
	buffer_load_dwordx4 v215, s[12:15], s16 offen lds
	s_mov_b32 m0, s64
	s_add_i32 s16, s47, 0x80000
	buffer_load_dwordx4 v214, s[8:11], s47 offen lds
	s_mov_b32 m0, s71
	s_nop 0
	buffer_load_dwordx4 v214, s[8:11], s16 offen lds
	s_lshl_b32 s99, s67, 10
	s_lshl_b32 s100, s95, 8
	s_or_b32 s99, s99, s100
	s_cmp_lg_u64 s[44:45], 0
	s_cselect_b32 s100, 8, 0
	s_or_b32 s99, s99, s100
	s_lshl_b32 s36, s36, 7
	s_mov_b32 s100, 0x1000
	s_mov_b32 s101, 0
	s_waitcnt vmcnt(10)
	s_waitcnt lgkmcnt(6)
	s_barrier
	s_setprio 1
	s_waitcnt lgkmcnt(7)
	v_mfma_f32_16x16x32_bf16 v[60:63], v[158:161], v[174:177], v[60:63]
	s_waitcnt lgkmcnt(6)
	v_mfma_f32_16x16x32_bf16 v[60:63], v[162:165], v[178:181], v[60:63]
	v_mfma_f32_16x16x32_bf16 v[56:59], v[166:169], v[174:177], v[56:59]
	v_lshlrev_b32_e32 v242, 3, v156
	v_mfma_f32_16x16x32_bf16 v[56:59], v[170:173], v[178:181], v[56:59]
	s_waitcnt lgkmcnt(5)
	v_mfma_f32_16x16x32_bf16 v[52:55], v[158:161], v[182:185], v[52:55]
	s_waitcnt lgkmcnt(4)
	v_mfma_f32_16x16x32_bf16 v[52:55], v[162:165], v[186:189], v[52:55]
	v_mfma_f32_16x16x32_bf16 v[48:51], v[166:169], v[182:185], v[48:51]
	v_and_b32_e32 v242, 0xf0, v242
	v_mfma_f32_16x16x32_bf16 v[48:51], v[170:173], v[186:189], v[48:51]
	s_waitcnt lgkmcnt(3)
	v_mfma_f32_16x16x32_bf16 v[44:47], v[158:161], v[190:193], v[44:47]
	s_waitcnt lgkmcnt(2)
	v_mfma_f32_16x16x32_bf16 v[44:47], v[162:165], v[194:197], v[44:47]
	v_mfma_f32_16x16x32_bf16 v[40:43], v[166:169], v[190:193], v[40:43]
	v_or_b32_e32 v242, s99, v242
	v_mfma_f32_16x16x32_bf16 v[40:43], v[170:173], v[194:197], v[40:43]
	s_waitcnt lgkmcnt(1)
	v_mfma_f32_16x16x32_bf16 v[36:39], v[158:161], v[234:237], v[36:39]
	s_waitcnt lgkmcnt(0)
	v_mfma_f32_16x16x32_bf16 v[36:39], v[162:165], v[238:241], v[36:39]
	v_mfma_f32_16x16x32_bf16 v[32:35], v[166:169], v[234:237], v[32:35]
	v_or_b32_e32 v204, v242, v202
	v_mfma_f32_16x16x32_bf16 v[32:35], v[170:173], v[238:241], v[32:35]
	s_setprio 0
	s_setprio 1
	v_mfma_f32_16x16x32_bf16 v[28:31], v[148:151], v[174:177], v[28:31]
	v_lshlrev_b64 v[242:243], 12, v[204:205]
	v_mfma_f32_16x16x32_bf16 v[28:31], v[144:147], v[178:181], v[28:31]
	v_mfma_f32_16x16x32_bf16 v[24:27], v[140:143], v[174:177], v[24:27]
	v_lshl_add_u64 v[242:243], s[6:7], 0, v[242:243]
	v_mfma_f32_16x16x32_bf16 v[24:27], v[136:139], v[178:181], v[24:27]
	v_mfma_f32_16x16x32_bf16 v[20:23], v[148:151], v[182:185], v[20:23]
	v_lshl_add_u64 v[242:243], v[242:243], 0, s[36:37]
	v_mfma_f32_16x16x32_bf16 v[20:23], v[144:147], v[186:189], v[20:23]
	v_mfma_f32_16x16x32_bf16 v[16:19], v[140:143], v[182:185], v[16:19]
	v_lshl_add_u64 v[242:243], v[242:243], 0, v[200:201]
	v_mfma_f32_16x16x32_bf16 v[16:19], v[136:139], v[186:189], v[16:19]
	v_mfma_f32_16x16x32_bf16 v[12:15], v[148:151], v[190:193], v[12:15]
	v_lshl_add_u64 v[244:245], v[242:243], 0, s[100:101]
	v_mfma_f32_16x16x32_bf16 v[12:15], v[144:147], v[194:197], v[12:15]
	v_mfma_f32_16x16x32_bf16 v[8:11], v[140:143], v[190:193], v[8:11]
	v_lshl_add_u64 v[246:247], v[244:245], 0, s[100:101]
	v_mfma_f32_16x16x32_bf16 v[8:11], v[136:139], v[194:197], v[8:11]
	v_mfma_f32_16x16x32_bf16 v[4:7], v[148:151], v[234:237], v[4:7]
	v_lshl_add_u64 v[254:255], v[246:247], 0, s[100:101]
	v_mfma_f32_16x16x32_bf16 v[4:7], v[144:147], v[238:241], v[4:7]
	v_mfma_f32_16x16x32_bf16 v[0:3], v[140:143], v[234:237], v[0:3]
	s_nop 0
	v_mfma_f32_16x16x32_bf16 v[0:3], v[136:139], v[238:241], v[0:3]
	s_setprio 0
	s_barrier
	ds_read_b128 v[136:139], v225
	ds_read_b128 v[140:143], v226
	ds_read_b128 v[144:147], v227
	ds_read_b128 v[148:151], v228
	ds_read_b128 v[158:161], v229
	ds_read_b128 v[162:165], v230
	ds_read_b128 v[166:169], v231
	ds_read_b128 v[170:173], v232
	ds_read_b128 v[174:177], v233 offset:32768
	ds_read_b128 v[178:181], v233 offset:33792
	ds_read_b128 v[182:185], v233 offset:34816
	ds_read_b128 v[186:189], v233 offset:35840
	ds_read_b128 v[190:193], v233 offset:36864
	ds_read_b128 v[194:197], v233 offset:37888
	ds_read_b128 v[234:237], v233 offset:38912
	ds_read_b128 v[238:241], v233 offset:39936
	s_mov_b32 m0, s72
	s_add_i32 s16, s47, 0x100000
	buffer_load_dwordx4 v214, s[8:11], s16 offen lds
	s_add_i32 s16, s47, 0x180000
	s_mov_b32 m0, s73
	s_nop 0
	buffer_load_dwordx4 v214, s[8:11], s16 offen lds
	s_waitcnt vmcnt(10)
	s_waitcnt lgkmcnt(8)
	s_barrier
	s_setprio 1
	s_waitcnt lgkmcnt(7)
	v_mfma_f32_16x16x32_bf16 v[124:127], v[136:139], v[174:177], v[124:127]
	s_waitcnt lgkmcnt(6)
	v_mfma_f32_16x16x32_bf16 v[124:127], v[140:143], v[178:181], v[124:127]
	v_mfma_f32_16x16x32_bf16 v[120:123], v[144:147], v[174:177], v[120:123]
	s_nop 0
	v_mfma_f32_16x16x32_bf16 v[120:123], v[148:151], v[178:181], v[120:123]
	s_waitcnt lgkmcnt(5)
	v_mfma_f32_16x16x32_bf16 v[116:119], v[136:139], v[182:185], v[116:119]
	s_waitcnt lgkmcnt(4)
	v_mfma_f32_16x16x32_bf16 v[116:119], v[140:143], v[186:189], v[116:119]
	v_mfma_f32_16x16x32_bf16 v[112:115], v[144:147], v[182:185], v[112:115]
	s_nop 0
	v_mfma_f32_16x16x32_bf16 v[112:115], v[148:151], v[186:189], v[112:115]
	s_waitcnt lgkmcnt(3)
	v_mfma_f32_16x16x32_bf16 v[108:111], v[136:139], v[190:193], v[108:111]
	s_waitcnt lgkmcnt(2)
	v_mfma_f32_16x16x32_bf16 v[108:111], v[140:143], v[194:197], v[108:111]
	v_mfma_f32_16x16x32_bf16 v[104:107], v[144:147], v[190:193], v[104:107]
	s_nop 0
	v_mfma_f32_16x16x32_bf16 v[104:107], v[148:151], v[194:197], v[104:107]
	s_waitcnt lgkmcnt(1)
	v_mfma_f32_16x16x32_bf16 v[100:103], v[136:139], v[234:237], v[100:103]
	s_waitcnt lgkmcnt(0)
	v_mfma_f32_16x16x32_bf16 v[100:103], v[140:143], v[238:241], v[100:103]
	v_mfma_f32_16x16x32_bf16 v[96:99], v[144:147], v[234:237], v[96:99]
	s_nop 0
	v_mfma_f32_16x16x32_bf16 v[96:99], v[148:151], v[238:241], v[96:99]
	s_setprio 0
	s_setprio 1
	v_mfma_f32_16x16x32_bf16 v[92:95], v[158:161], v[174:177], v[92:95]
	s_nop 0
	v_mfma_f32_16x16x32_bf16 v[92:95], v[162:165], v[178:181], v[92:95]
	v_mfma_f32_16x16x32_bf16 v[88:91], v[166:169], v[174:177], v[88:91]
	s_nop 0
	v_mfma_f32_16x16x32_bf16 v[88:91], v[170:173], v[178:181], v[88:91]
	v_mfma_f32_16x16x32_bf16 v[84:87], v[158:161], v[182:185], v[84:87]
	s_nop 0
	v_mfma_f32_16x16x32_bf16 v[84:87], v[162:165], v[186:189], v[84:87]
	v_mfma_f32_16x16x32_bf16 v[80:83], v[166:169], v[182:185], v[80:83]
	s_nop 0
	v_mfma_f32_16x16x32_bf16 v[80:83], v[170:173], v[186:189], v[80:83]
	v_mfma_f32_16x16x32_bf16 v[76:79], v[158:161], v[190:193], v[76:79]
	s_nop 0
	v_mfma_f32_16x16x32_bf16 v[76:79], v[162:165], v[194:197], v[76:79]
	v_mfma_f32_16x16x32_bf16 v[72:75], v[166:169], v[190:193], v[72:75]
	s_nop 0
	v_mfma_f32_16x16x32_bf16 v[72:75], v[170:173], v[194:197], v[72:75]
	v_mfma_f32_16x16x32_bf16 v[68:71], v[158:161], v[234:237], v[68:71]
	s_nop 0
	v_mfma_f32_16x16x32_bf16 v[68:71], v[162:165], v[238:241], v[68:71]
	v_mfma_f32_16x16x32_bf16 v[64:67], v[166:169], v[234:237], v[64:67]
	s_nop 0
	v_mfma_f32_16x16x32_bf16 v[64:67], v[170:173], v[238:241], v[64:67]
	s_setprio 0
	s_barrier
	ds_read_b128 v[174:177], v233 offset:49152
	ds_read_b128 v[178:181], v233 offset:50176
	ds_read_b128 v[182:185], v233 offset:51200
	ds_read_b128 v[186:189], v233 offset:52224
	ds_read_b128 v[190:193], v233 offset:53248
	ds_read_b128 v[194:197], v233 offset:54272
	ds_read_b128 v[234:237], v233 offset:55296
	ds_read_b128 v[238:241], v233 offset:56320
	s_mov_b32 m0, s76
	s_add_i32 s16, s97, 0x100080
	buffer_load_dwordx4 v215, s[12:15], vcc_lo offen lds
	s_mov_b32 m0, s77
	s_add_i32 s47, s47, 0x80080
	buffer_load_dwordx4 v215, s[12:15], s16 offen lds
	s_add_i32 s16, s97, 0x10080
	s_mov_b32 m0, s80
	s_add_i32 s97, s97, 0x110080
	buffer_load_dwordx4 v215, s[12:15], s16 offen lds
	s_mov_b32 m0, s81
	s_nop 0
	buffer_load_dwordx4 v215, s[12:15], s97 offen lds
	s_mov_b32 m0, s78
	s_nop 0
	buffer_load_dwordx4 v214, s[8:11], s96 offen lds
	s_mov_b32 m0, s79
	s_nop 0
	buffer_load_dwordx4 v214, s[8:11], s47 offen lds
	s_bitcmp0_b32 s46, 0
	s_mov_b32 s98, 0xffff
	s_cselect_b32 s98, 0xffff0000, s98
	s_waitcnt vmcnt(8)
	s_waitcnt lgkmcnt(6)
	s_barrier
	s_setprio 1
	s_waitcnt lgkmcnt(7)
	v_mfma_f32_16x16x32_bf16 v[60:63], v[136:139], v[174:177], v[60:63]
	s_waitcnt lgkmcnt(6)
	v_mfma_f32_16x16x32_bf16 v[60:63], v[140:143], v[178:181], v[60:63]
	v_mfma_f32_16x16x32_bf16 v[56:59], v[144:147], v[174:177], v[56:59]
	v_mul_f32_e32 v128, 0x42800000, v128
	v_mfma_f32_16x16x32_bf16 v[56:59], v[148:151], v[178:181], v[56:59]
	v_mul_f32_e32 v130, 0x42800000, v130
	s_waitcnt lgkmcnt(5)
	v_mfma_f32_16x16x32_bf16 v[52:55], v[136:139], v[182:185], v[52:55]
	s_waitcnt lgkmcnt(4)
	v_mfma_f32_16x16x32_bf16 v[52:55], v[140:143], v[186:189], v[52:55]
	v_mfma_f32_16x16x32_bf16 v[48:51], v[144:147], v[182:185], v[48:51]
	v_mul_f32_e32 v132, 0x42800000, v132
	v_mfma_f32_16x16x32_bf16 v[48:51], v[148:151], v[186:189], v[48:51]
	v_mul_f32_e32 v134, 0x42800000, v134
	s_waitcnt lgkmcnt(3)
	v_mfma_f32_16x16x32_bf16 v[44:47], v[136:139], v[190:193], v[44:47]
	s_waitcnt lgkmcnt(2)
	v_mfma_f32_16x16x32_bf16 v[44:47], v[140:143], v[194:197], v[44:47]
	v_mfma_f32_16x16x32_bf16 v[40:43], v[144:147], v[190:193], v[40:43]
	v_mul_f32_e32 v129, 0x42800000, v129
	v_mfma_f32_16x16x32_bf16 v[40:43], v[148:151], v[194:197], v[40:43]
	v_mul_f32_e32 v131, 0x42800000, v131
	s_waitcnt lgkmcnt(1)
	v_mfma_f32_16x16x32_bf16 v[36:39], v[136:139], v[234:237], v[36:39]
	s_waitcnt lgkmcnt(0)
	v_mfma_f32_16x16x32_bf16 v[36:39], v[140:143], v[238:241], v[36:39]
	v_mfma_f32_16x16x32_bf16 v[32:35], v[144:147], v[234:237], v[32:35]
	v_mul_f32_e32 v133, 0x42800000, v133
	v_mfma_f32_16x16x32_bf16 v[32:35], v[148:151], v[238:241], v[32:35]
	v_mul_f32_e32 v135, 0x42800000, v135
	s_setprio 0
	s_setprio 1
	v_mfma_f32_16x16x32_bf16 v[28:31], v[158:161], v[174:177], v[28:31]
	v_cvt_pk_fp8_f32 v204, v128, v132
	v_mfma_f32_16x16x32_bf16 v[28:31], v[162:165], v[178:181], v[28:31]
	v_mfma_f32_16x16x32_bf16 v[24:27], v[166:169], v[174:177], v[24:27]
	v_cvt_pk_fp8_f32 v204, v128, v132 op_sel:[0,0,1]
	v_mfma_f32_16x16x32_bf16 v[24:27], v[170:173], v[178:181], v[24:27]
	v_mfma_f32_16x16x32_bf16 v[20:23], v[158:161], v[182:185], v[20:23]
	v_cvt_pk_fp8_f32 v250, v129, v133
	v_mfma_f32_16x16x32_bf16 v[20:23], v[162:165], v[186:189], v[20:23]
	v_mfma_f32_16x16x32_bf16 v[16:19], v[166:169], v[182:185], v[16:19]
	v_cvt_pk_fp8_f32 v250, v129, v133 op_sel:[0,0,1]
	v_mfma_f32_16x16x32_bf16 v[16:19], v[170:173], v[186:189], v[16:19]
	v_mfma_f32_16x16x32_bf16 v[12:15], v[158:161], v[190:193], v[12:15]
	v_cvt_pk_fp8_f32 v251, v130, v134
	v_mfma_f32_16x16x32_bf16 v[12:15], v[162:165], v[194:197], v[12:15]
	v_bfi_b32 v152, s98, v204, v152
	v_mfma_f32_16x16x32_bf16 v[8:11], v[166:169], v[190:193], v[8:11]
	v_cvt_pk_fp8_f32 v251, v130, v134 op_sel:[0,0,1]
	v_mfma_f32_16x16x32_bf16 v[8:11], v[170:173], v[194:197], v[8:11]
	v_bfi_b32 v153, s98, v250, v153
	v_mfma_f32_16x16x32_bf16 v[4:7], v[158:161], v[234:237], v[4:7]
	v_cvt_pk_fp8_f32 v252, v131, v135
	v_mfma_f32_16x16x32_bf16 v[4:7], v[162:165], v[238:241], v[4:7]
	v_bfi_b32 v154, s98, v251, v154
	v_mfma_f32_16x16x32_bf16 v[0:3], v[166:169], v[234:237], v[0:3]
	v_cvt_pk_fp8_f32 v252, v131, v135 op_sel:[0,0,1]
	v_mfma_f32_16x16x32_bf16 v[0:3], v[170:173], v[238:241], v[0:3]
	v_bfi_b32 v155, s98, v252, v155
	s_setprio 0
	s_barrier
	s_bitcmp0_b32 s46, 0
	s_mov_b64 s[46:47], -1
	s_cbranch_scc0 .LBB0_345
	s_andn2_b64 vcc, exec, s[4:5]
	s_cbranch_vccnz .LBB0_345
	global_store_dword v[242:243], v152, off
	global_store_dword v[244:245], v153, off
	global_store_dword v[246:247], v154, off
	global_store_dword v[254:255], v155, off
	s_branch .LBB0_345
